# MoE gather phase: per-wave expert prefix sums from one 64-lane load + DPP/readlane reduction instead of 8 serialized per-expert load loops; on top of indexer packed keys
# baseline (speedup 1.0000x reference)
.LBB0_1805:
	s_or_b64 exec, exec, s[10:11]
	s_ashr_i32 s3, s3, 6
	s_cmp_gt_i32 s3, 0
	s_cselect_b64 s[12:13], -1, 0
	s_add_u32 s14, s64, 0x184000
	s_addc_u32 s15, s65, 0
	s_lshl_b32 s16, s62, 6
	s_cmp_lt_i32 s3, 1
	s_waitcnt vmcnt(1)
	v_mov_b32_e32 v4, 0
	v_mov_b32_e32 v2, 0
	s_waitcnt lgkmcnt(0)
	s_barrier
	v_and_b32_e32 v68, 63, v0
	v_lshlrev_b32_e32 v69, 2, v68
	s_lshl_b32 s0, s16, 2
	s_add_u32 s0, s14, s0
	s_addc_u32 s1, s15, 0
	global_load_dword v70, v69, s[0:1]
	v_lshrrev_b32_e32 v68, 3, v68
	v_cmp_gt_u32_e32 vcc, s3, v68
	s_waitcnt vmcnt(0)
	v_cndmask_b32_e32 v70, 0, v70, vcc
	s_nop 1
	v_add_u32_dpp v70, v70, v70 row_shr:8 row_mask:0xf bank_mask:0xf bound_ctrl:1
	s_nop 1
	v_readlane_b32 s0, v70, 8
	v_readlane_b32 s1, v70, 24
	v_readlane_b32 s10, v70, 40
	v_readlane_b32 s11, v70, 56
	s_add_i32 s0, s0, s1
	s_add_i32 s10, s10, s11
	s_add_i32 s0, s0, s10
	v_mov_b32_e32 v60, s0
	v_readlane_b32 s0, v70, 9
	v_readlane_b32 s1, v70, 25
	v_readlane_b32 s10, v70, 41
	v_readlane_b32 s11, v70, 57
	s_add_i32 s0, s0, s1
	s_add_i32 s10, s10, s11
	s_add_i32 s0, s0, s10
	v_mov_b32_e32 v61, s0
	v_readlane_b32 s0, v70, 10
	v_readlane_b32 s1, v70, 26
	v_readlane_b32 s10, v70, 42
	v_readlane_b32 s11, v70, 58
	s_add_i32 s0, s0, s1
	s_add_i32 s10, s10, s11
	s_add_i32 s0, s0, s10
	v_mov_b32_e32 v62, s0
	v_readlane_b32 s0, v70, 11
	v_readlane_b32 s1, v70, 27
	v_readlane_b32 s10, v70, 43
	v_readlane_b32 s11, v70, 59
	s_add_i32 s0, s0, s1
	s_add_i32 s10, s10, s11
	s_add_i32 s0, s0, s10
	v_mov_b32_e32 v63, s0
	v_readlane_b32 s0, v70, 12
	v_readlane_b32 s1, v70, 28
	v_readlane_b32 s10, v70, 44
	v_readlane_b32 s11, v70, 60
	s_add_i32 s0, s0, s1
	s_add_i32 s10, s10, s11
	s_add_i32 s0, s0, s10
	v_mov_b32_e32 v64, s0
	v_readlane_b32 s0, v70, 13
	v_readlane_b32 s1, v70, 29
	v_readlane_b32 s10, v70, 45
	v_readlane_b32 s11, v70, 61
	s_add_i32 s0, s0, s1
	s_add_i32 s10, s10, s11
	s_add_i32 s0, s0, s10
	v_mov_b32_e32 v65, s0
	v_readlane_b32 s0, v70, 14
	v_readlane_b32 s1, v70, 30
	v_readlane_b32 s10, v70, 46
	v_readlane_b32 s11, v70, 62
	s_add_i32 s0, s0, s1
	s_add_i32 s10, s10, s11
	s_add_i32 s0, s0, s10
	v_mov_b32_e32 v66, s0
	v_readlane_b32 s0, v70, 15
	v_readlane_b32 s1, v70, 31
	v_readlane_b32 s10, v70, 47
	v_readlane_b32 s11, v70, 63
	s_add_i32 s0, s0, s1
	s_add_i32 s10, s10, s11
	s_add_i32 s0, s0, s10
	v_mov_b32_e32 v67, s0
	v_mov_b32_e32 v2, v60
	s_branch .LBB0_1815
	s_cmp_lt_u32 s3, 18
	s_cselect_b64 s[0:1], -1, 0
	s_and_b64 vcc, exec, s[0:1]
	s_cbranch_vccnz .LBB0_1812
	s_add_i32 s0, s3, -1
	s_lshl_b32 s10, s0, 3
	s_cmp_lt_u32 s0, 0x20000000
	s_cselect_b64 s[0:1], -1, 0
	s_add_i32 s10, s16, s10
	s_cmp_ge_i32 s10, s16
	s_cselect_b64 s[10:11], -1, 0
	s_and_b64 s[0:1], s[10:11], s[0:1]
	s_and_b64 vcc, exec, s[0:1]
	s_cbranch_vccz .LBB0_1811
	s_and_b32 s10, s3, 0x3ffffffe
	s_mov_b32 s0, s16
	s_mov_b32 s1, 1
	s_mov_b32 s11, 0
	v_mov_b32_e32 v2, 0
	v_mov_b32_e32 v5, 0
	s_mov_b32 s17, s10

.LBB0_1815:
	s_add_i32 s0, 0, 0x20200
	v_mov_b32_e32 v5, s0
	v_readlane_b32 s0, v254, 25
	v_cndmask_b32_e64 v7, 0, 1, s[12:13]
	v_cmp_ne_u32_e64 s[10:11], 1, v7
	v_mov_b32_e32 v6, s0
	ds_read_b32 v5, v5
	ds_read_b32 v6, v6
	s_andn2_b64 vcc, exec, s[12:13]
	v_mov_b32_e32 v4, v61
	s_branch .LBB0_1825
	s_cmp_lt_u32 s3, 18
	s_cselect_b64 s[0:1], -1, 0
	s_and_b64 vcc, exec, s[0:1]
	s_cbranch_vccnz .LBB0_1822
	s_add_i32 s1, s3, -1
	s_or_b32 s0, s16, 1
	s_lshl_b32 s17, s1, 3
	s_cmp_lt_u32 s1, 0x20000000
	s_cselect_b64 s[12:13], -1, 0
	s_add_i32 s1, s0, s17
	s_cmp_gt_i32 s1, s16
	s_cselect_b64 s[18:19], -1, 0
	s_and_b64 s[12:13], s[18:19], s[12:13]
	s_and_b64 vcc, exec, s[12:13]
	s_cbranch_vccz .LBB0_1821
	s_and_b32 s12, s3, 0x3ffffffe
	s_mov_b32 s1, s0
	s_mov_b32 s13, 1
	s_mov_b32 s17, 0
	v_mov_b32_e32 v4, 0
	v_mov_b32_e32 v7, 0
	s_mov_b32 s18, s12

.LBB0_1825:
	v_readlane_b32 s0, v254, 9
	s_and_b64 vcc, exec, s[10:11]
	s_waitcnt vmcnt(0)
	v_mov_b32_e32 v10, 0
	v_mov_b32_e32 v7, s0
	v_readlane_b32 s0, v254, 37
	v_mov_b32_e32 v9, 0
	s_nop 0
	v_mov_b32_e32 v8, s0
	ds_read_b32 v7, v7
	ds_read_b32 v8, v8
	v_mov_b32_e32 v9, v62
	s_branch .LBB0_1835
	s_cmp_lt_u32 s3, 18
	s_cselect_b64 s[0:1], -1, 0
	s_and_b64 vcc, exec, s[0:1]
	s_cbranch_vccnz .LBB0_1832
	s_add_i32 s1, s3, -1
	s_or_b32 s0, s16, 2
	s_lshl_b32 s17, s1, 3
	s_cmp_lt_u32 s1, 0x20000000
	s_cselect_b64 s[12:13], -1, 0
	s_add_i32 s1, s0, s17
	s_cmp_gt_i32 s1, s16
	s_cselect_b64 s[18:19], -1, 0
	s_and_b64 s[12:13], s[18:19], s[12:13]
	s_and_b64 vcc, exec, s[12:13]
	s_cbranch_vccz .LBB0_1831
	s_and_b32 s12, s3, 0x3ffffffe
	s_mov_b32 s1, s0
	s_mov_b32 s13, 1
	s_mov_b32 s17, 0
	v_mov_b32_e32 v9, 0
	v_mov_b32_e32 v11, 0
	s_mov_b32 s18, s12

.LBB0_1835:
	v_readlane_b32 s0, v254, 38
	s_and_b64 vcc, exec, s[10:11]
	s_nop 0
	v_mov_b32_e32 v11, s0
	v_readlane_b32 s0, v254, 39
	s_nop 1
	v_mov_b32_e32 v12, s0
	ds_read_b32 v11, v11
	ds_read_b32 v12, v12
	v_mov_b32_e32 v10, v63
	s_branch .LBB0_1845
	s_cmp_lt_u32 s3, 18
	s_cselect_b64 s[0:1], -1, 0
	s_and_b64 vcc, exec, s[0:1]
	s_cbranch_vccnz .LBB0_1842
	s_add_i32 s1, s3, -1
	s_or_b32 s0, s16, 3
	s_lshl_b32 s17, s1, 3
	s_cmp_lt_u32 s1, 0x20000000
	s_cselect_b64 s[12:13], -1, 0
	s_add_i32 s1, s0, s17
	s_cmp_ge_i32 s1, s0
	s_cselect_b64 s[18:19], -1, 0
	s_and_b64 s[12:13], s[18:19], s[12:13]
	s_and_b64 vcc, exec, s[12:13]
	s_cbranch_vccz .LBB0_1841
	s_and_b32 s12, s3, 0x3ffffffe
	s_mov_b32 s1, s0
	s_mov_b32 s13, 1
	s_mov_b32 s17, 0
	v_mov_b32_e32 v10, 0
	v_mov_b32_e32 v13, 0
	s_mov_b32 s18, s12

.LBB0_1845:
	v_readlane_b32 s0, v254, 10
	s_and_b64 vcc, exec, s[10:11]
	v_mov_b32_e32 v15, 0
	v_mov_b32_e32 v13, s0
	v_readlane_b32 s0, v254, 40
	v_mov_b32_e32 v16, 0
	s_nop 0
	v_mov_b32_e32 v14, s0
	ds_read_b32 v13, v13
	ds_read_b32 v17, v14
	v_mov_b32_e32 v16, v64
	s_branch .LBB0_1855
	s_cmp_lt_u32 s3, 18
	s_cselect_b64 s[0:1], -1, 0
	s_and_b64 vcc, exec, s[0:1]
	s_cbranch_vccnz .LBB0_1852
	s_add_i32 s1, s3, -1
	s_or_b32 s0, s16, 4
	s_lshl_b32 s17, s1, 3
	s_cmp_lt_u32 s1, 0x20000000
	s_cselect_b64 s[12:13], -1, 0
	s_add_i32 s1, s0, s17
	s_cmp_gt_i32 s1, s16
	s_cselect_b64 s[18:19], -1, 0
	s_and_b64 s[12:13], s[18:19], s[12:13]
	s_and_b64 vcc, exec, s[12:13]
	s_cbranch_vccz .LBB0_1851
	s_and_b32 s12, s3, 0x3ffffffe
	s_mov_b32 s1, s0
	s_mov_b32 s13, 1
	s_mov_b32 s17, 0
	v_mov_b32_e32 v14, 0
	v_mov_b32_e32 v16, 0
	s_mov_b32 s18, s12

.LBB0_1855:
	v_readlane_b32 s0, v254, 34
	s_and_b64 vcc, exec, s[10:11]
	s_nop 0
	v_mov_b32_e32 v14, s0
	v_readlane_b32 s0, v254, 35
	s_nop 1
	v_mov_b32_e32 v19, s0
	ds_read_b32 v18, v14
	ds_read_b32 v19, v19
	v_mov_b32_e32 v15, v65
	s_branch .LBB0_1865
	s_cmp_lt_u32 s3, 18
	s_cselect_b64 s[0:1], -1, 0
	s_and_b64 vcc, exec, s[0:1]
	s_cbranch_vccnz .LBB0_1862
	s_add_i32 s1, s3, -1
	s_or_b32 s0, s16, 5
	s_lshl_b32 s17, s1, 3
	s_cmp_lt_u32 s1, 0x20000000
	s_cselect_b64 s[12:13], -1, 0
	s_add_i32 s1, s0, s17
	s_cmp_ge_i32 s1, s0
	s_cselect_b64 s[18:19], -1, 0
	s_and_b64 s[12:13], s[18:19], s[12:13]
	s_and_b64 vcc, exec, s[12:13]
	s_cbranch_vccz .LBB0_1861
	s_and_b32 s12, s3, 0x3ffffffe
	s_mov_b32 s1, s0
	s_mov_b32 s13, 1
	s_mov_b32 s17, 0
	v_mov_b32_e32 v14, 0
	v_mov_b32_e32 v15, 0
	s_mov_b32 s18, s12

.LBB0_1865:
	v_readlane_b32 s0, v254, 11
	s_and_b64 vcc, exec, s[10:11]
	v_mov_b32_e32 v22, 0
	v_mov_b32_e32 v14, s0
	v_readlane_b32 s0, v254, 41
	s_nop 1
	v_mov_b32_e32 v21, s0
	ds_read_b32 v20, v14
	ds_read_b32 v21, v21
	v_mov_b32_e32 v14, 0
	v_mov_b32_e32 v14, v66
	s_branch .LBB0_1875
	s_cmp_lt_u32 s3, 18
	s_cselect_b64 s[0:1], -1, 0
	s_and_b64 vcc, exec, s[0:1]
	s_cbranch_vccnz .LBB0_1872
	s_add_i32 s1, s3, -1
	s_or_b32 s0, s16, 6
	s_lshl_b32 s17, s1, 3
	s_cmp_lt_u32 s1, 0x20000000
	s_cselect_b64 s[12:13], -1, 0
	s_add_i32 s1, s0, s17
	s_cmp_ge_i32 s1, s0
	s_cselect_b64 s[18:19], -1, 0
	s_and_b64 s[12:13], s[18:19], s[12:13]
	s_and_b64 vcc, exec, s[12:13]
	s_cbranch_vccz .LBB0_1871
	s_and_b32 s12, s3, 0x3ffffffe
	s_mov_b32 s1, s0
	s_mov_b32 s13, 1
	s_mov_b32 s17, 0
	v_mov_b32_e32 v14, 0
	v_mov_b32_e32 v23, 0
	s_mov_b32 s18, s12

.LBB0_1875:
	v_readlane_b32 s0, v254, 42
	s_and_b64 vcc, exec, s[10:11]
	s_nop 0
	v_mov_b32_e32 v23, s0
	v_readlane_b32 s0, v254, 43
	s_nop 1
	v_mov_b32_e32 v24, s0
	ds_read_b32 v23, v23
	ds_read_b32 v24, v24
	v_mov_b32_e32 v22, v67
	s_branch .LBB0_1885
	s_cmp_lt_u32 s3, 18
	s_cselect_b64 s[0:1], -1, 0
	s_and_b64 vcc, exec, s[0:1]
	s_cbranch_vccnz .LBB0_1882
	s_add_i32 s1, s3, -1
	s_or_b32 s0, s16, 7
	s_lshl_b32 s12, s1, 3
	s_cmp_lt_u32 s1, 0x20000000
	s_cselect_b64 s[10:11], -1, 0
	s_add_i32 s1, s0, s12
	s_cmp_ge_i32 s1, s0
	s_cselect_b64 s[12:13], -1, 0
	s_and_b64 s[10:11], s[12:13], s[10:11]
	s_and_b64 vcc, exec, s[10:11]
	s_cbranch_vccz .LBB0_1881
	s_and_b32 s10, s3, 0x3ffffffe
	s_mov_b32 s1, s0
	s_mov_b32 s11, 1
	s_mov_b32 s12, 0
	v_mov_b32_e32 v22, 0
	v_mov_b32_e32 v25, 0
	s_mov_b32 s13, s10
